# grid barrier: waiting workgroups poll the top-level generation word directly instead of the per-XCD generation word (one hop less)
# speedup vs baseline: 1.0347x; 1.0022x over previous
; __device__ __forceinline__ unsigned xb_ld(unsigned* p)              { return __hip_atomic_load(p, __ATOMIC_RELAXED, __HIP_MEMORY_SCOPE_AGENT); }
; __device__ __forceinline__ unsigned xb_add(unsigned* p, unsigned v) { return __hip_atomic_fetch_add(p, v, __ATOMIC_RELAXED, __HIP_MEMORY_SCOPE_AGENT); }
; #define XB_SPIN(cond, bar) do { unsigned _sp = 0; while (cond) { __builtin_amdgcn_s_sleep(1); \
;     if ((++_sp & 255u) == 0u) { if (xb_ld(&(bar)[XB_TMO])) break; if (_sp > XB_SPIN_CAP) { atomicAdd(&(bar)[XB_TMO], 1u); break; } } } } while (0)
; __device__ __forceinline__ void xcd_barrier(const XcdBarrier& b, bool leader) {
;     ...
;         const unsigned old = xb_add(&bar[XB_XSUB(b.x)], 1u);
;         const unsigned gen = old / nloc;
;         if (old + 1u == (gen + 1u) * nloc) {
;             __builtin_amdgcn_fence(__ATOMIC_RELEASE, "agent");
;             asm volatile("s_waitcnt vmcnt(0)" ::: "memory");
;             const unsigned og = xb_add(&bar[XB_TOP], 1u);
;             const unsigned tg = og / nx;
;             if (og + 1u == (tg + 1u) * nx) xb_add(&bar[XB_TOPGEN], 1u);
;             else XB_SPIN(xb_ld(&bar[XB_TOPGEN]) == tg, bar);
;             __builtin_amdgcn_fence(__ATOMIC_ACQUIRE, "agent");
;             xb_add(&bar[XB_XGEN(b.x)], 1u);
;             asm volatile("s_waitcnt vmcnt(0)" ::: "memory");
;         } else {
;             XB_SPIN(xb_ld(&bar[XB_XGEN(b.x)]) == gen, bar);
.LBB0_291:
	s_or_b64 exec, exec, s[2:3]
	v_cvt_f32_u32_e32 v4, v2
	s_waitcnt vmcnt(0)
	v_readfirstlane_b32 s2, v3
	v_sub_u32_e32 v3, 0, v2
	v_rcp_iflag_f32_e32 v4, v4
	v_add_u32_e32 v5, s2, v1
	v_mul_f32_e32 v4, 0x4f7ffffe, v4
	v_cvt_u32_f32_e32 v4, v4
	v_mul_lo_u32 v1, v3, v4
	v_mul_hi_u32 v1, v4, v1
	v_add_u32_e32 v1, v4, v1
	v_mul_hi_u32 v1, v5, v1
	v_mul_lo_u32 v3, v1, v2
	v_sub_u32_e32 v3, v5, v3
	v_add_u32_e32 v4, 1, v1
	v_cmp_ge_u32_e32 vcc, v3, v2
	s_nop 1
	v_cndmask_b32_e32 v1, v1, v4, vcc
	v_sub_u32_e32 v4, v3, v2
	v_cndmask_b32_e32 v3, v3, v4, vcc
	v_add_u32_e32 v4, 1, v1
	v_cmp_ge_u32_e32 vcc, v3, v2
	v_add_u32_e32 v3, 1, v5
	s_nop 0
	v_cndmask_b32_e32 v1, v1, v4, vcc
	v_mul_lo_u32 v4, v2, v1
	v_add_u32_e32 v2, v4, v2
	v_cmp_ne_u32_e32 vcc, v3, v2
	s_and_saveexec_b64 s[2:3], vcc
	s_xor_b64 s[2:3], exec, s[2:3]
	s_cbranch_execz .LBB0_307
	v_readlane_b32 s4, v253, 15
	s_waitcnt lgkmcnt(0)
	v_mov_b32_e32 v0, 0
	v_readlane_b32 s5, v253, 16
	s_nop 4
	global_load_dword v2, v0, s[4:5] sc1
	s_waitcnt vmcnt(0)
	v_cmp_eq_u32_e32 vcc, v2, v1
	s_and_saveexec_b64 s[4:5], vcc
	s_cbranch_execz .LBB0_306
	s_mov_b32 s16, 1
	s_mov_b64 s[6:7], 0
	s_branch .LBB0_295

; __device__ __forceinline__ unsigned xb_ld(unsigned* p)              { return __hip_atomic_load(p, __ATOMIC_RELAXED, __HIP_MEMORY_SCOPE_AGENT); }
; #define XB_SPIN(cond, bar) do { unsigned _sp = 0; while (cond) { __builtin_amdgcn_s_sleep(1); \
;     if ((++_sp & 255u) == 0u) { if (xb_ld(&(bar)[XB_TMO])) break; if (_sp > XB_SPIN_CAP) { atomicAdd(&(bar)[XB_TMO], 1u); break; } } } } while (0)
; __device__ __forceinline__ void xcd_barrier(const XcdBarrier& b, bool leader) {
;     ...
;             XB_SPIN(xb_ld(&bar[XB_XGEN(b.x)]) == gen, bar);
.LBB0_299:
	v_readlane_b32 s10, v253, 15
	v_readlane_b32 s11, v253, 16
	s_add_i32 s16, s16, 1
	s_mov_b64 s[12:13], -1
	s_nop 2
	global_load_dword v2, v0, s[10:11] sc1
	s_waitcnt vmcnt(0)
	v_cmp_ne_u32_e32 vcc, v2, v1
	s_orn2_b64 s[10:11], vcc, exec
	s_branch .LBB0_294

; __device__ __forceinline__ unsigned xb_ld(unsigned* p)              { return __hip_atomic_load(p, __ATOMIC_RELAXED, __HIP_MEMORY_SCOPE_AGENT); }
; __device__ __forceinline__ unsigned xb_add(unsigned* p, unsigned v) { return __hip_atomic_fetch_add(p, v, __ATOMIC_RELAXED, __HIP_MEMORY_SCOPE_AGENT); }
; #define XB_SPIN(cond, bar) do { unsigned _sp = 0; while (cond) { __builtin_amdgcn_s_sleep(1); \
;     if ((++_sp & 255u) == 0u) { if (xb_ld(&(bar)[XB_TMO])) break; if (_sp > XB_SPIN_CAP) { atomicAdd(&(bar)[XB_TMO], 1u); break; } } } } while (0)
; __device__ __forceinline__ void xcd_barrier(const XcdBarrier& b, bool leader) {
;     ...
;         const unsigned old = xb_add(&bar[XB_XSUB(b.x)], 1u);
;         const unsigned gen = old / nloc;
;         if (old + 1u == (gen + 1u) * nloc) {
;             __builtin_amdgcn_fence(__ATOMIC_RELEASE, "agent");
;             asm volatile("s_waitcnt vmcnt(0)" ::: "memory");
;             const unsigned og = xb_add(&bar[XB_TOP], 1u);
;             const unsigned tg = og / nx;
;             if (og + 1u == (tg + 1u) * nx) xb_add(&bar[XB_TOPGEN], 1u);
;             else XB_SPIN(xb_ld(&bar[XB_TOPGEN]) == tg, bar);
;             __builtin_amdgcn_fence(__ATOMIC_ACQUIRE, "agent");
;             xb_add(&bar[XB_XGEN(b.x)], 1u);
;             asm volatile("s_waitcnt vmcnt(0)" ::: "memory");
;         } else {
;             XB_SPIN(xb_ld(&bar[XB_XGEN(b.x)]) == gen, bar);
.LBB0_377:
	s_or_b64 exec, exec, s[10:11]
	v_cvt_f32_u32_e32 v4, v2
	s_waitcnt vmcnt(0)
	v_readfirstlane_b32 s10, v3
	v_sub_u32_e32 v3, 0, v2
	v_rcp_iflag_f32_e32 v4, v4
	v_add_u32_e32 v5, s10, v1
	v_mul_f32_e32 v4, 0x4f7ffffe, v4
	v_cvt_u32_f32_e32 v4, v4
	v_mul_lo_u32 v1, v3, v4
	v_mul_hi_u32 v1, v4, v1
	v_add_u32_e32 v1, v4, v1
	v_mul_hi_u32 v1, v5, v1
	v_mul_lo_u32 v3, v1, v2
	v_sub_u32_e32 v3, v5, v3
	v_add_u32_e32 v4, 1, v1
	v_cmp_ge_u32_e32 vcc, v3, v2
	s_nop 1
	v_cndmask_b32_e32 v1, v1, v4, vcc
	v_sub_u32_e32 v4, v3, v2
	v_cndmask_b32_e32 v3, v3, v4, vcc
	v_add_u32_e32 v4, 1, v1
	v_cmp_ge_u32_e32 vcc, v3, v2
	v_add_u32_e32 v3, 1, v5
	s_nop 0
	v_cndmask_b32_e32 v1, v1, v4, vcc
	v_mul_lo_u32 v4, v2, v1
	v_add_u32_e32 v2, v4, v2
	v_cmp_ne_u32_e32 vcc, v3, v2
	s_and_saveexec_b64 s[10:11], vcc
	s_xor_b64 s[10:11], exec, s[10:11]
	s_cbranch_execz .LBB0_391
	v_readlane_b32 s22, v253, 15
	v_readlane_b32 s23, v253, 16
	s_waitcnt lgkmcnt(0)
	s_nop 3
	global_load_dword v0, v169, s[22:23] sc1
	s_waitcnt vmcnt(0)
	v_cmp_eq_u32_e32 vcc, v0, v1
	s_and_saveexec_b64 s[22:23], vcc
	s_cbranch_execz .LBB0_390
	s_mov_b32 s42, 1
	s_mov_b64 s[30:31], 0
	s_branch .LBB0_381

; __device__ __forceinline__ unsigned xb_ld(unsigned* p)              { return __hip_atomic_load(p, __ATOMIC_RELAXED, __HIP_MEMORY_SCOPE_AGENT); }
; #define XB_SPIN(cond, bar) do { unsigned _sp = 0; while (cond) { __builtin_amdgcn_s_sleep(1); \
;     if ((++_sp & 255u) == 0u) { if (xb_ld(&(bar)[XB_TMO])) break; if (_sp > XB_SPIN_CAP) { atomicAdd(&(bar)[XB_TMO], 1u); break; } } } } while (0)
; __device__ __forceinline__ void xcd_barrier(const XcdBarrier& b, bool leader) {
;     ...
;             XB_SPIN(xb_ld(&bar[XB_XGEN(b.x)]) == gen, bar);
.LBB0_385:
	v_readlane_b32 s36, v253, 15
	v_readlane_b32 s37, v253, 16
	s_add_i32 s42, s42, 1
	s_mov_b64 s[38:39], -1
	s_nop 2
	global_load_dword v0, v169, s[36:37] sc1
	s_waitcnt vmcnt(0)
	v_cmp_ne_u32_e32 vcc, v0, v1
	s_orn2_b64 s[36:37], vcc, exec
	s_branch .LBB0_380

; __device__ __forceinline__ unsigned xb_ld(unsigned* p)              { return __hip_atomic_load(p, __ATOMIC_RELAXED, __HIP_MEMORY_SCOPE_AGENT); }
; __device__ __forceinline__ unsigned xb_add(unsigned* p, unsigned v) { return __hip_atomic_fetch_add(p, v, __ATOMIC_RELAXED, __HIP_MEMORY_SCOPE_AGENT); }
; #define XB_SPIN(cond, bar) do { unsigned _sp = 0; while (cond) { __builtin_amdgcn_s_sleep(1); \
;     if ((++_sp & 255u) == 0u) { if (xb_ld(&(bar)[XB_TMO])) break; if (_sp > XB_SPIN_CAP) { atomicAdd(&(bar)[XB_TMO], 1u); break; } } } } while (0)
; __device__ __forceinline__ void xcd_barrier(const XcdBarrier& b, bool leader) {
;     ...
;         const unsigned old = xb_add(&bar[XB_XSUB(b.x)], 1u);
;         const unsigned gen = old / nloc;
;         if (old + 1u == (gen + 1u) * nloc) {
;             __builtin_amdgcn_fence(__ATOMIC_RELEASE, "agent");
;             asm volatile("s_waitcnt vmcnt(0)" ::: "memory");
;             const unsigned og = xb_add(&bar[XB_TOP], 1u);
;             const unsigned tg = og / nx;
;             if (og + 1u == (tg + 1u) * nx) xb_add(&bar[XB_TOPGEN], 1u);
;             else XB_SPIN(xb_ld(&bar[XB_TOPGEN]) == tg, bar);
;             __builtin_amdgcn_fence(__ATOMIC_ACQUIRE, "agent");
;             xb_add(&bar[XB_XGEN(b.x)], 1u);
;             asm volatile("s_waitcnt vmcnt(0)" ::: "memory");
;         } else {
;             XB_SPIN(xb_ld(&bar[XB_XGEN(b.x)]) == gen, bar);
.LBB0_519:
	s_or_b64 exec, exec, s[12:13]
	v_cvt_f32_u32_e32 v4, v2
	s_waitcnt vmcnt(0)
	v_readfirstlane_b32 s12, v3
	v_sub_u32_e32 v3, 0, v2
	v_rcp_iflag_f32_e32 v4, v4
	v_add_u32_e32 v5, s12, v1
	v_mul_f32_e32 v4, 0x4f7ffffe, v4
	v_cvt_u32_f32_e32 v4, v4
	v_mul_lo_u32 v1, v3, v4
	v_mul_hi_u32 v1, v4, v1
	v_add_u32_e32 v1, v4, v1
	v_mul_hi_u32 v1, v5, v1
	v_mul_lo_u32 v3, v1, v2
	v_sub_u32_e32 v3, v5, v3
	v_add_u32_e32 v4, 1, v1
	v_cmp_ge_u32_e32 vcc, v3, v2
	s_nop 1
	v_cndmask_b32_e32 v1, v1, v4, vcc
	v_sub_u32_e32 v4, v3, v2
	v_cndmask_b32_e32 v3, v3, v4, vcc
	v_add_u32_e32 v4, 1, v1
	v_cmp_ge_u32_e32 vcc, v3, v2
	v_add_u32_e32 v3, 1, v5
	s_nop 0
	v_cndmask_b32_e32 v1, v1, v4, vcc
	v_mul_lo_u32 v4, v2, v1
	v_add_u32_e32 v2, v4, v2
	v_cmp_ne_u32_e32 vcc, v3, v2
	s_and_saveexec_b64 s[12:13], vcc
	s_xor_b64 s[12:13], exec, s[12:13]
	s_cbranch_execz .LBB0_533
	v_readlane_b32 s22, v253, 15
	v_readlane_b32 s23, v253, 16
	s_waitcnt lgkmcnt(0)
	s_nop 3
	global_load_dword v0, v169, s[22:23] sc1
	s_waitcnt vmcnt(0)
	v_cmp_eq_u32_e32 vcc, v0, v1
	s_and_saveexec_b64 s[22:23], vcc
	s_cbranch_execz .LBB0_532
	s_mov_b32 s17, 1
	s_mov_b64 s[30:31], 0
	s_branch .LBB0_523

; __device__ __forceinline__ unsigned xb_ld(unsigned* p)              { return __hip_atomic_load(p, __ATOMIC_RELAXED, __HIP_MEMORY_SCOPE_AGENT); }
; #define XB_SPIN(cond, bar) do { unsigned _sp = 0; while (cond) { __builtin_amdgcn_s_sleep(1); \
;     if ((++_sp & 255u) == 0u) { if (xb_ld(&(bar)[XB_TMO])) break; if (_sp > XB_SPIN_CAP) { atomicAdd(&(bar)[XB_TMO], 1u); break; } } } } while (0)
; __device__ __forceinline__ void xcd_barrier(const XcdBarrier& b, bool leader) {
;     ...
;             XB_SPIN(xb_ld(&bar[XB_XGEN(b.x)]) == gen, bar);
.LBB0_527:
	v_readlane_b32 s36, v253, 15
	v_readlane_b32 s37, v253, 16
	s_add_i32 s17, s17, 1
	s_mov_b64 s[38:39], -1
	s_nop 2
	global_load_dword v0, v169, s[36:37] sc1
	s_waitcnt vmcnt(0)
	v_cmp_ne_u32_e32 vcc, v0, v1
	s_orn2_b64 s[36:37], vcc, exec
	s_branch .LBB0_522

; __device__ __forceinline__ unsigned xb_ld(unsigned* p)              { return __hip_atomic_load(p, __ATOMIC_RELAXED, __HIP_MEMORY_SCOPE_AGENT); }
; __device__ __forceinline__ unsigned xb_add(unsigned* p, unsigned v) { return __hip_atomic_fetch_add(p, v, __ATOMIC_RELAXED, __HIP_MEMORY_SCOPE_AGENT); }
; #define XB_SPIN(cond, bar) do { unsigned _sp = 0; while (cond) { __builtin_amdgcn_s_sleep(1); \
;     if ((++_sp & 255u) == 0u) { if (xb_ld(&(bar)[XB_TMO])) break; if (_sp > XB_SPIN_CAP) { atomicAdd(&(bar)[XB_TMO], 1u); break; } } } } while (0)
; __device__ __forceinline__ void xcd_barrier(const XcdBarrier& b, bool leader) {
;     ...
;         const unsigned old = xb_add(&bar[XB_XSUB(b.x)], 1u);
;         const unsigned gen = old / nloc;
;         if (old + 1u == (gen + 1u) * nloc) {
;             __builtin_amdgcn_fence(__ATOMIC_RELEASE, "agent");
;             asm volatile("s_waitcnt vmcnt(0)" ::: "memory");
;             const unsigned og = xb_add(&bar[XB_TOP], 1u);
;             const unsigned tg = og / nx;
;             if (og + 1u == (tg + 1u) * nx) xb_add(&bar[XB_TOPGEN], 1u);
;             else XB_SPIN(xb_ld(&bar[XB_TOPGEN]) == tg, bar);
;             __builtin_amdgcn_fence(__ATOMIC_ACQUIRE, "agent");
;             xb_add(&bar[XB_XGEN(b.x)], 1u);
;             asm volatile("s_waitcnt vmcnt(0)" ::: "memory");
;         } else {
;             XB_SPIN(xb_ld(&bar[XB_XGEN(b.x)]) == gen, bar);
.LBB0_599:
	s_or_b64 exec, exec, s[10:11]
	v_cvt_f32_u32_e32 v4, v2
	s_waitcnt vmcnt(0)
	v_readfirstlane_b32 s10, v3
	v_sub_u32_e32 v3, 0, v2
	v_rcp_iflag_f32_e32 v4, v4
	v_add_u32_e32 v5, s10, v1
	v_mul_f32_e32 v4, 0x4f7ffffe, v4
	v_cvt_u32_f32_e32 v4, v4
	v_mul_lo_u32 v1, v3, v4
	v_mul_hi_u32 v1, v4, v1
	v_add_u32_e32 v1, v4, v1
	v_mul_hi_u32 v1, v5, v1
	v_mul_lo_u32 v3, v1, v2
	v_sub_u32_e32 v3, v5, v3
	v_add_u32_e32 v4, 1, v1
	v_cmp_ge_u32_e32 vcc, v3, v2
	s_nop 1
	v_cndmask_b32_e32 v1, v1, v4, vcc
	v_sub_u32_e32 v4, v3, v2
	v_cndmask_b32_e32 v3, v3, v4, vcc
	v_add_u32_e32 v4, 1, v1
	v_cmp_ge_u32_e32 vcc, v3, v2
	v_add_u32_e32 v3, 1, v5
	s_nop 0
	v_cndmask_b32_e32 v1, v1, v4, vcc
	v_mul_lo_u32 v4, v2, v1
	v_add_u32_e32 v2, v4, v2
	v_cmp_ne_u32_e32 vcc, v3, v2
	s_and_saveexec_b64 s[10:11], vcc
	s_xor_b64 s[10:11], exec, s[10:11]
	s_cbranch_execz .LBB0_613
	v_readlane_b32 s12, v253, 15
	v_readlane_b32 s13, v253, 16
	s_waitcnt lgkmcnt(0)
	s_nop 3
	global_load_dword v0, v169, s[12:13] sc1
	s_waitcnt vmcnt(0)
	v_cmp_eq_u32_e32 vcc, v0, v1
	s_and_saveexec_b64 s[12:13], vcc
	s_cbranch_execz .LBB0_612
	s_mov_b32 s38, 1
	s_mov_b64 s[14:15], 0
	s_branch .LBB0_603

; __device__ __forceinline__ unsigned xb_ld(unsigned* p)              { return __hip_atomic_load(p, __ATOMIC_RELAXED, __HIP_MEMORY_SCOPE_AGENT); }
; #define XB_SPIN(cond, bar) do { unsigned _sp = 0; while (cond) { __builtin_amdgcn_s_sleep(1); \
;     if ((++_sp & 255u) == 0u) { if (xb_ld(&(bar)[XB_TMO])) break; if (_sp > XB_SPIN_CAP) { atomicAdd(&(bar)[XB_TMO], 1u); break; } } } } while (0)
; __device__ __forceinline__ void xcd_barrier(const XcdBarrier& b, bool leader) {
;     ...
;             XB_SPIN(xb_ld(&bar[XB_XGEN(b.x)]) == gen, bar);
.LBB0_607:
	v_readlane_b32 s30, v253, 15
	v_readlane_b32 s31, v253, 16
	s_add_i32 s38, s38, 1
	s_mov_b64 s[34:35], -1
	s_nop 2
	global_load_dword v0, v169, s[30:31] sc1
	s_waitcnt vmcnt(0)
	v_cmp_ne_u32_e32 vcc, v0, v1
	s_orn2_b64 s[30:31], vcc, exec
	s_branch .LBB0_602

; __device__ __forceinline__ unsigned xb_ld(unsigned* p)              { return __hip_atomic_load(p, __ATOMIC_RELAXED, __HIP_MEMORY_SCOPE_AGENT); }
; __device__ __forceinline__ unsigned xb_add(unsigned* p, unsigned v) { return __hip_atomic_fetch_add(p, v, __ATOMIC_RELAXED, __HIP_MEMORY_SCOPE_AGENT); }
; #define XB_SPIN(cond, bar) do { unsigned _sp = 0; while (cond) { __builtin_amdgcn_s_sleep(1); \
;     if ((++_sp & 255u) == 0u) { if (xb_ld(&(bar)[XB_TMO])) break; if (_sp > XB_SPIN_CAP) { atomicAdd(&(bar)[XB_TMO], 1u); break; } } } } while (0)
; __device__ __forceinline__ void xcd_barrier(const XcdBarrier& b, bool leader) {
;     ...
;         const unsigned old = xb_add(&bar[XB_XSUB(b.x)], 1u);
;         const unsigned gen = old / nloc;
;         if (old + 1u == (gen + 1u) * nloc) {
;             __builtin_amdgcn_fence(__ATOMIC_RELEASE, "agent");
;             asm volatile("s_waitcnt vmcnt(0)" ::: "memory");
;             const unsigned og = xb_add(&bar[XB_TOP], 1u);
;             const unsigned tg = og / nx;
;             if (og + 1u == (tg + 1u) * nx) xb_add(&bar[XB_TOPGEN], 1u);
;             else XB_SPIN(xb_ld(&bar[XB_TOPGEN]) == tg, bar);
;             __builtin_amdgcn_fence(__ATOMIC_ACQUIRE, "agent");
;             xb_add(&bar[XB_XGEN(b.x)], 1u);
;             asm volatile("s_waitcnt vmcnt(0)" ::: "memory");
;         } else {
;             XB_SPIN(xb_ld(&bar[XB_XGEN(b.x)]) == gen, bar);
.LBB0_675:
	s_or_b64 exec, exec, s[12:13]
	v_cvt_f32_u32_e32 v4, v2
	s_waitcnt vmcnt(0)
	v_readfirstlane_b32 s12, v3
	v_sub_u32_e32 v3, 0, v2
	v_rcp_iflag_f32_e32 v4, v4
	v_add_u32_e32 v5, s12, v1
	v_mul_f32_e32 v4, 0x4f7ffffe, v4
	v_cvt_u32_f32_e32 v4, v4
	v_mul_lo_u32 v1, v3, v4
	v_mul_hi_u32 v1, v4, v1
	v_add_u32_e32 v1, v4, v1
	v_mul_hi_u32 v1, v5, v1
	v_mul_lo_u32 v3, v1, v2
	v_sub_u32_e32 v3, v5, v3
	v_add_u32_e32 v4, 1, v1
	v_cmp_ge_u32_e32 vcc, v3, v2
	s_nop 1
	v_cndmask_b32_e32 v1, v1, v4, vcc
	v_sub_u32_e32 v4, v3, v2
	v_cndmask_b32_e32 v3, v3, v4, vcc
	v_add_u32_e32 v4, 1, v1
	v_cmp_ge_u32_e32 vcc, v3, v2
	v_add_u32_e32 v3, 1, v5
	s_nop 0
	v_cndmask_b32_e32 v1, v1, v4, vcc
	v_mul_lo_u32 v4, v2, v1
	v_add_u32_e32 v2, v4, v2
	v_cmp_ne_u32_e32 vcc, v3, v2
	s_and_saveexec_b64 s[12:13], vcc
	s_xor_b64 s[12:13], exec, s[12:13]
	s_cbranch_execz .LBB0_689
	v_readlane_b32 s22, v253, 15
	v_readlane_b32 s23, v253, 16
	s_waitcnt lgkmcnt(0)
	s_nop 3
	global_load_dword v0, v169, s[22:23] sc1
	s_waitcnt vmcnt(0)
	v_cmp_eq_u32_e32 vcc, v0, v1
	s_and_saveexec_b64 s[22:23], vcc
	s_cbranch_execz .LBB0_688
	s_mov_b32 s27, 1
	s_mov_b64 s[30:31], 0
	s_branch .LBB0_679

; __device__ __forceinline__ unsigned xb_ld(unsigned* p)              { return __hip_atomic_load(p, __ATOMIC_RELAXED, __HIP_MEMORY_SCOPE_AGENT); }
; #define XB_SPIN(cond, bar) do { unsigned _sp = 0; while (cond) { __builtin_amdgcn_s_sleep(1); \
;     if ((++_sp & 255u) == 0u) { if (xb_ld(&(bar)[XB_TMO])) break; if (_sp > XB_SPIN_CAP) { atomicAdd(&(bar)[XB_TMO], 1u); break; } } } } while (0)
; __device__ __forceinline__ void xcd_barrier(const XcdBarrier& b, bool leader) {
;     ...
;             XB_SPIN(xb_ld(&bar[XB_XGEN(b.x)]) == gen, bar);
.LBB0_683:
	v_readlane_b32 s36, v253, 15
	v_readlane_b32 s37, v253, 16
	s_add_i32 s27, s27, 1
	s_mov_b64 s[38:39], -1
	s_nop 2
	global_load_dword v0, v169, s[36:37] sc1
	s_waitcnt vmcnt(0)
	v_cmp_ne_u32_e32 vcc, v0, v1
	s_orn2_b64 s[36:37], vcc, exec
	s_branch .LBB0_678

; __device__ __forceinline__ unsigned xb_ld(unsigned* p)              { return __hip_atomic_load(p, __ATOMIC_RELAXED, __HIP_MEMORY_SCOPE_AGENT); }
; __device__ __forceinline__ unsigned xb_add(unsigned* p, unsigned v) { return __hip_atomic_fetch_add(p, v, __ATOMIC_RELAXED, __HIP_MEMORY_SCOPE_AGENT); }
; #define XB_SPIN(cond, bar) do { unsigned _sp = 0; while (cond) { __builtin_amdgcn_s_sleep(1); \
;     if ((++_sp & 255u) == 0u) { if (xb_ld(&(bar)[XB_TMO])) break; if (_sp > XB_SPIN_CAP) { atomicAdd(&(bar)[XB_TMO], 1u); break; } } } } while (0)
; __device__ __forceinline__ void xcd_barrier(const XcdBarrier& b, bool leader) {
;     ...
;         const unsigned old = xb_add(&bar[XB_XSUB(b.x)], 1u);
;         const unsigned gen = old / nloc;
;         if (old + 1u == (gen + 1u) * nloc) {
;             __builtin_amdgcn_fence(__ATOMIC_RELEASE, "agent");
;             asm volatile("s_waitcnt vmcnt(0)" ::: "memory");
;             const unsigned og = xb_add(&bar[XB_TOP], 1u);
;             const unsigned tg = og / nx;
;             if (og + 1u == (tg + 1u) * nx) xb_add(&bar[XB_TOPGEN], 1u);
;             else XB_SPIN(xb_ld(&bar[XB_TOPGEN]) == tg, bar);
;             __builtin_amdgcn_fence(__ATOMIC_ACQUIRE, "agent");
;             xb_add(&bar[XB_XGEN(b.x)], 1u);
;             asm volatile("s_waitcnt vmcnt(0)" ::: "memory");
;         } else {
;             XB_SPIN(xb_ld(&bar[XB_XGEN(b.x)]) == gen, bar);
.LBB0_1017:
	s_or_b64 exec, exec, s[10:11]
	v_cvt_f32_u32_e32 v4, v2
	s_waitcnt vmcnt(0)
	v_readfirstlane_b32 s10, v3
	v_sub_u32_e32 v3, 0, v2
	v_rcp_iflag_f32_e32 v4, v4
	v_add_u32_e32 v5, s10, v1
	v_mul_f32_e32 v4, 0x4f7ffffe, v4
	v_cvt_u32_f32_e32 v4, v4
	v_mul_lo_u32 v1, v3, v4
	v_mul_hi_u32 v1, v4, v1
	v_add_u32_e32 v1, v4, v1
	v_mul_hi_u32 v1, v5, v1
	v_mul_lo_u32 v3, v1, v2
	v_sub_u32_e32 v3, v5, v3
	v_add_u32_e32 v4, 1, v1
	v_cmp_ge_u32_e32 vcc, v3, v2
	s_nop 1
	v_cndmask_b32_e32 v1, v1, v4, vcc
	v_sub_u32_e32 v4, v3, v2
	v_cndmask_b32_e32 v3, v3, v4, vcc
	v_add_u32_e32 v4, 1, v1
	v_cmp_ge_u32_e32 vcc, v3, v2
	v_add_u32_e32 v3, 1, v5
	s_nop 0
	v_cndmask_b32_e32 v1, v1, v4, vcc
	v_mul_lo_u32 v4, v2, v1
	v_add_u32_e32 v2, v4, v2
	v_cmp_ne_u32_e32 vcc, v3, v2
	s_and_saveexec_b64 s[10:11], vcc
	s_xor_b64 s[10:11], exec, s[10:11]
	s_cbranch_execz .LBB0_1031
	v_readlane_b32 s14, v253, 15
	v_readlane_b32 s15, v253, 16
	s_waitcnt lgkmcnt(0)
	s_nop 3
	global_load_dword v0, v169, s[14:15] sc1
	s_waitcnt vmcnt(0)
	v_cmp_eq_u32_e32 vcc, v0, v1
	s_and_saveexec_b64 s[14:15], vcc
	s_cbranch_execz .LBB0_1030
	s_mov_b32 s40, 1
	s_mov_b64 s[22:23], 0
	s_branch .LBB0_1021

; __device__ __forceinline__ unsigned xb_ld(unsigned* p)              { return __hip_atomic_load(p, __ATOMIC_RELAXED, __HIP_MEMORY_SCOPE_AGENT); }
; #define XB_SPIN(cond, bar) do { unsigned _sp = 0; while (cond) { __builtin_amdgcn_s_sleep(1); \
;     if ((++_sp & 255u) == 0u) { if (xb_ld(&(bar)[XB_TMO])) break; if (_sp > XB_SPIN_CAP) { atomicAdd(&(bar)[XB_TMO], 1u); break; } } } } while (0)
; __device__ __forceinline__ void xcd_barrier(const XcdBarrier& b, bool leader) {
;     ...
;             XB_SPIN(xb_ld(&bar[XB_XGEN(b.x)]) == gen, bar);
.LBB0_1025:
	v_readlane_b32 s34, v253, 15
	v_readlane_b32 s35, v253, 16
	s_add_i32 s40, s40, 1
	s_mov_b64 s[36:37], -1
	s_nop 2
	global_load_dword v0, v169, s[34:35] sc1
	s_waitcnt vmcnt(0)
	v_cmp_ne_u32_e32 vcc, v0, v1
	s_orn2_b64 s[34:35], vcc, exec
	s_branch .LBB0_1020

; __device__ __forceinline__ unsigned xb_ld(unsigned* p)              { return __hip_atomic_load(p, __ATOMIC_RELAXED, __HIP_MEMORY_SCOPE_AGENT); }
; __device__ __forceinline__ unsigned xb_add(unsigned* p, unsigned v) { return __hip_atomic_fetch_add(p, v, __ATOMIC_RELAXED, __HIP_MEMORY_SCOPE_AGENT); }
; #define XB_SPIN(cond, bar) do { unsigned _sp = 0; while (cond) { __builtin_amdgcn_s_sleep(1); \
;     if ((++_sp & 255u) == 0u) { if (xb_ld(&(bar)[XB_TMO])) break; if (_sp > XB_SPIN_CAP) { atomicAdd(&(bar)[XB_TMO], 1u); break; } } } } while (0)
; __device__ __forceinline__ void xcd_barrier(const XcdBarrier& b, bool leader) {
;     ...
;         const unsigned old = xb_add(&bar[XB_XSUB(b.x)], 1u);
;         const unsigned gen = old / nloc;
;         if (old + 1u == (gen + 1u) * nloc) {
;             __builtin_amdgcn_fence(__ATOMIC_RELEASE, "agent");
;             asm volatile("s_waitcnt vmcnt(0)" ::: "memory");
;             const unsigned og = xb_add(&bar[XB_TOP], 1u);
;             const unsigned tg = og / nx;
;             if (og + 1u == (tg + 1u) * nx) xb_add(&bar[XB_TOPGEN], 1u);
;             else XB_SPIN(xb_ld(&bar[XB_TOPGEN]) == tg, bar);
;             __builtin_amdgcn_fence(__ATOMIC_ACQUIRE, "agent");
;             xb_add(&bar[XB_XGEN(b.x)], 1u);
;             asm volatile("s_waitcnt vmcnt(0)" ::: "memory");
;         } else {
;             XB_SPIN(xb_ld(&bar[XB_XGEN(b.x)]) == gen, bar);
.LBB0_1097:
	s_or_b64 exec, exec, s[10:11]
	v_cvt_f32_u32_e32 v4, v2
	s_waitcnt vmcnt(0)
	v_readfirstlane_b32 s10, v3
	v_sub_u32_e32 v3, 0, v2
	v_rcp_iflag_f32_e32 v4, v4
	v_add_u32_e32 v5, s10, v1
	v_mul_f32_e32 v4, 0x4f7ffffe, v4
	v_cvt_u32_f32_e32 v4, v4
	v_mul_lo_u32 v1, v3, v4
	v_mul_hi_u32 v1, v4, v1
	v_add_u32_e32 v1, v4, v1
	v_mul_hi_u32 v1, v5, v1
	v_mul_lo_u32 v3, v1, v2
	v_sub_u32_e32 v3, v5, v3
	v_add_u32_e32 v4, 1, v1
	v_cmp_ge_u32_e32 vcc, v3, v2
	s_nop 1
	v_cndmask_b32_e32 v1, v1, v4, vcc
	v_sub_u32_e32 v4, v3, v2
	v_cndmask_b32_e32 v3, v3, v4, vcc
	v_add_u32_e32 v4, 1, v1
	v_cmp_ge_u32_e32 vcc, v3, v2
	v_add_u32_e32 v3, 1, v5
	s_nop 0
	v_cndmask_b32_e32 v1, v1, v4, vcc
	v_mul_lo_u32 v4, v2, v1
	v_add_u32_e32 v2, v4, v2
	v_cmp_ne_u32_e32 vcc, v3, v2
	s_and_saveexec_b64 s[10:11], vcc
	s_xor_b64 s[10:11], exec, s[10:11]
	s_cbranch_execz .LBB0_1111
	v_readlane_b32 s12, v253, 15
	v_readlane_b32 s13, v253, 16
	s_waitcnt lgkmcnt(0)
	s_nop 3
	global_load_dword v0, v169, s[12:13] sc1
	s_waitcnt vmcnt(0)
	v_cmp_eq_u32_e32 vcc, v0, v1
	s_and_saveexec_b64 s[12:13], vcc
	s_cbranch_execz .LBB0_1110
	s_mov_b32 s17, 1
	s_mov_b64 s[14:15], 0
	s_branch .LBB0_1101

; __device__ __forceinline__ unsigned xb_ld(unsigned* p)              { return __hip_atomic_load(p, __ATOMIC_RELAXED, __HIP_MEMORY_SCOPE_AGENT); }
; #define XB_SPIN(cond, bar) do { unsigned _sp = 0; while (cond) { __builtin_amdgcn_s_sleep(1); \
;     if ((++_sp & 255u) == 0u) { if (xb_ld(&(bar)[XB_TMO])) break; if (_sp > XB_SPIN_CAP) { atomicAdd(&(bar)[XB_TMO], 1u); break; } } } } while (0)
; __device__ __forceinline__ void xcd_barrier(const XcdBarrier& b, bool leader) {
;     ...
;             XB_SPIN(xb_ld(&bar[XB_XGEN(b.x)]) == gen, bar);
.LBB0_1105:
	v_readlane_b32 s30, v253, 15
	v_readlane_b32 s31, v253, 16
	s_add_i32 s17, s17, 1
	s_mov_b64 s[34:35], -1
	s_nop 2
	global_load_dword v0, v169, s[30:31] sc1
	s_waitcnt vmcnt(0)
	v_cmp_ne_u32_e32 vcc, v0, v1
	s_orn2_b64 s[30:31], vcc, exec
	s_branch .LBB0_1100
